# baseline (speedup 1.0000x reference)
_Z11lstm_kernelPKiPKhPKfS4_S4_Pf:
	s_load_dwordx4 s[12:15], s[0:1], 0x0
	v_readfirstlane_b32 s19, v0
	v_or_b32_e32 v3, 0x400, v0
	s_movk_i32 s4, 0x500
	s_lshr_b32 s7, s19, 6
	s_lshl_b32 s18, s2, 6
	s_mulk_i32 s2, 0x1400
	v_mov_b32_e32 v2, 0x4ff
	v_cmp_gt_u32_e32 vcc, s4, v3
	s_mul_hi_i32 s3, s18, 0x50
	s_waitcnt lgkmcnt(0)
	s_add_u32 s2, s12, s2
	v_cndmask_b32_e32 v2, v2, v3, vcc
	s_addc_u32 s3, s13, s3
	v_lshlrev_b32_e32 v1, 2, v0
	v_lshlrev_b32_e32 v4, 2, v2
	s_movk_i32 s4, 0x184
	v_or_b32_e32 v28, 0x200, v0
	global_load_dword v29, v1, s[2:3]
	global_load_dword v30, v1, s[2:3] offset:2048
	global_load_dword v2, v4, s[2:3]
	v_mov_b32_e32 v4, 0x383
	v_cmp_gt_u32_e32 vcc, s4, v0
	s_add_u32 s2, s14, 0x34000
	s_addc_u32 s3, s15, 0
	v_cndmask_b32_e32 v4, v4, v28, vcc
	v_lshlrev_b32_e32 v31, 4, v0
	v_lshlrev_b32_e32 v4, 4, v4
	global_load_dwordx4 v[6:9], v31, s[2:3]
	global_load_dwordx4 v[10:13], v4, s[2:3]
	v_and_b32_e32 v4, 0x7f, v0
	v_lshlrev_b32_e32 v18, 4, v4
	v_mov_b32_e32 v19, 0
	v_lshl_add_u64 v[4:5], s[14:15], 0, v[18:19]
	s_mov_b32 s2, 0x37000
	v_add_co_u32_e64 v4, s[2:3], s2, v4
	s_nop 1
	v_addc_co_u32_e64 v5, s[2:3], 0, v5, s[2:3]
	global_load_dwordx4 v[14:17], v[4:5], off offset:2112
	s_movk_i32 s22, 0x410
	s_movk_i32 s2, 0x4ff
	v_and_b32_e32 v4, 63, v0
	v_cmp_lt_u32_e64 s[2:3], s2, v3
	s_mul_i32 s5, s7, 0x6000
	s_mul_hi_u32 s4, s7, 0x6000
	s_add_u32 s8, s14, s5
	s_addc_u32 s9, s15, s4
	v_lshlrev_b32_e32 v210, 4, v4
	v_mov_b32_e32 v211, v19
	v_lshl_add_u64 v[20:21], s[8:9], 0, v[210:211]
	s_movk_i32 s4, 0x2000
	v_add_co_u32_e64 v22, s[4:5], s4, v20
	s_nop 1
	v_addc_co_u32_e64 v23, s[4:5], 0, v21, s[4:5]
	s_movk_i32 s4, 0x3000
	s_nop 0
	v_add_co_u32_e64 v24, s[4:5], s4, v20
	global_load_dwordx4 v[90:93], v[22:23], off offset:1024
	global_load_dwordx4 v[86:89], v[22:23], off offset:2048
	v_addc_co_u32_e64 v25, s[4:5], 0, v21, s[4:5]
	s_movk_i32 s4, 0x5000
	s_nop 0
	v_add_co_u32_e64 v26, s[4:5], s4, v20
	s_nop 1
	v_addc_co_u32_e64 v27, s[4:5], 0, v21, s[4:5]
	global_load_dwordx4 v[82:85], v[22:23], off offset:3072
	global_load_dwordx4 v[46:49], v[26:27], off
	global_load_dwordx4 v[42:45], v[26:27], off offset:1024
	global_load_dwordx4 v[38:41], v[26:27], off offset:2048
	global_load_dwordx4 v[94:97], v[24:25], off offset:-4096
	global_load_dwordx4 v[34:37], v[26:27], off offset:3072
	s_movk_i32 s4, 0x1000
	v_add_co_u32_e64 v22, s[4:5], s4, v20
	global_load_dwordx4 v[126:129], v210, s[8:9]
	global_load_dwordx4 v[122:125], v210, s[8:9] offset:1024
	global_load_dwordx4 v[118:121], v210, s[8:9] offset:2048
	global_load_dwordx4 v[114:117], v210, s[8:9] offset:3072
	v_addc_co_u32_e64 v23, s[4:5], 0, v21, s[4:5]
	global_load_dwordx4 v[110:113], v[22:23], off
	global_load_dwordx4 v[106:109], v[22:23], off offset:1024
	global_load_dwordx4 v[102:105], v[22:23], off offset:2048
	global_load_dwordx4 v[98:101], v[22:23], off offset:3072
	global_load_dwordx4 v[78:81], v[24:25], off
	global_load_dwordx4 v[74:77], v[24:25], off offset:1024
	global_load_dwordx4 v[70:73], v[24:25], off offset:2048
	global_load_dwordx4 v[66:69], v[24:25], off offset:3072
	s_movk_i32 s4, 0x4000
	v_add_co_u32_e64 v20, s[4:5], s4, v20
	v_mov_b32_e32 v5, 0x4000
	s_nop 0
	v_addc_co_u32_e64 v21, s[4:5], 0, v21, s[4:5]
	global_load_dwordx4 v[62:65], v[20:21], off
	global_load_dwordx4 v[58:61], v[20:21], off offset:1024
	global_load_dwordx4 v[54:57], v[20:21], off offset:2048
	global_load_dwordx4 v[50:53], v[20:21], off offset:3072
	s_waitcnt vmcnt(26)
	ds_write_b128 v31, v[6:9] offset:16384
	v_lshl_or_b32 v5, v28, 4, v5
	v_add_u32_e32 v6, 0x9840, v31
	v_cndmask_b32_e32 v5, v6, v5, vcc
	s_waitcnt vmcnt(25)
	ds_write_b128 v5, v[10:13]
	s_waitcnt vmcnt(24)
	ds_write_b128 v18, v[14:17] offset:36928
	v_mul_u32_u24_e32 v5, 0xccd, v0
	v_lshrrev_b32_e32 v5, 16, v5
	s_mov_b32 s5, 0xffffec
	v_mul_u32_u24_e32 v6, 0xccd, v28
	s_movk_i32 s4, 0x90
	v_mad_u32_u24 v8, v5, s5, v0
	v_lshlrev_b32_e32 v5, 2, v5
	v_lshrrev_b32_e32 v6, 16, v6
	v_mul_lo_u32 v7, v29, s4
	v_lshl_or_b32 v5, v8, 8, v5
	ds_write_b32 v5, v7 offset:30784
	v_mul_lo_u32 v196, v29, s22
	v_add_u32_e32 v197, 0x24e80, v5
	ds_write_b32 v197, v196
	v_mad_u32_u24 v7, v6, s5, v28
	v_lshlrev_b32_e32 v6, 2, v6
	v_mul_lo_u32 v5, v30, s4
	v_lshl_or_b32 v6, v7, 8, v6
	ds_write_b32 v6, v5 offset:30784
	v_mul_lo_u32 v198, v30, s22
	v_add_u32_e32 v199, 0x24e80, v6
	ds_write_b32 v199, v198
	s_and_saveexec_b64 s[4:5], s[2:3]
	s_xor_b64 s[2:3], exec, s[4:5]
	v_mov_b32_e32 v3, 0x9840
	v_lshl_add_u32 v5, v0, 2, v3
	s_andn2_saveexec_b64 s[2:3], s[2:3]
	v_mul_u32_u24_e32 v5, 0xccd, v3
	s_mov_b32 s4, 0xffffec
	v_mul_u32_u24_sdwa v6, v5, s4 dst_sel:DWORD dst_unused:UNUSED_PAD src0_sel:WORD_1 src1_sel:DWORD
	v_add_lshl_u32 v3, v6, v3, 8
	v_mov_b32_e32 v6, 2
	v_lshlrev_b32_sdwa v5, v6, v5 dst_sel:DWORD dst_unused:UNUSED_PAD src0_sel:DWORD src1_sel:WORD_1
	s_movk_i32 s4, 0x7840
	v_add3_u32 v5, v5, v3, s4
	s_or_b64 exec, exec, s[2:3]
	v_lshrrev_b32_e32 v3, 5, v4
	s_movk_i32 s2, 0x90
	s_lshl_b32 s6, s7, 10
	s_mulk_i32 s7, 0xfd00
	v_and_b32_e32 v182, 31, v0
	v_mul_lo_u32 v200, v2, s22
	v_mul_lo_u32 v2, v2, s2
	s_add_i32 s7, s6, s7
	v_lshlrev_b32_e32 v229, 6, v3
	ds_write_b32 v5, v2
	v_add_u32_e32 v201, 0x1d640, v5
	ds_write_b32 v201, v200
	v_lshlrev_b32_e32 v230, 4, v3
	v_lshlrev_b32_e32 v228, 2, v182
	v_or_b32_e32 v2, s7, v229
	s_waitcnt lgkmcnt(0)
	s_barrier
	s_cmpk_lt_u32 s19, 0x100
	s_cbranch_scc1 .Llight_path
	s_mov_b32 s12, 0xbeb17218
	v_add_u32_e32 v3, 0x7800, v228
	ds_read2_b32 v[138:139], v3 offset0:16 offset1:48
	ds_read_b128 v[18:21], v2 offset:36928
	ds_read_b128 v[22:25], v2 offset:36944
	s_waitcnt lgkmcnt(2)
	v_add_u32_e32 v3, v230, v138
	ds_read_b128 v[26:29], v2 offset:36960
	ds_read_b128 v[30:33], v2 offset:36976
	ds_read_b128 v[142:145], v3 offset:16384
	ds_read_b128 v[130:133], v3 offset:16416
	ds_read_b128 v[154:157], v3 offset:16448
	ds_read_b128 v[134:137], v3 offset:16480
	ds_read_b128 v[248:251], v2 offset:37104
	ds_read_b128 v[244:247], v2 offset:37088
	ds_read_b128 v[240:243], v2 offset:37072
	ds_read_b128 v[236:239], v2 offset:37056
	s_waitcnt vmcnt(17) lgkmcnt(7)
	v_mfma_f32_32x32x16_bf16 v[18:33], v[94:97], v[142:145], v[18:33]
	s_waitcnt lgkmcnt(6)
	v_mfma_f32_32x32x16_bf16 v[18:33], v[90:93], v[130:133], v[18:33]
	s_waitcnt lgkmcnt(5)
	v_mfma_f32_32x32x16_bf16 v[18:33], v[86:89], v[154:157], v[18:33]
	s_waitcnt lgkmcnt(4)
	v_mfma_f32_32x32x16_bf16 v[18:33], v[82:85], v[134:137], v[18:33]
	s_cmpk_lt_u32 s19, 0x100
	s_cselect_b64 s[2:3], -1, 0
	ds_read_b32 v158, v228 offset:31040
	v_add_u32_e32 v159, v230, v139
	s_nop 2
	v_exp_f32_e32 v139, v20
	v_exp_f32_e32 v138, v24
	v_exp_f32_e32 v141, v28
	v_exp_f32_e32 v140, v32
	v_exp_f32_e32 v18, v18
	v_exp_f32_e32 v20, v22
	v_exp_f32_e32 v22, v26
	v_add_f32_e32 v24, 1.0, v138
	v_add_f32_e32 v26, 1.0, v141
	v_add_f32_e32 v19, 1.0, v139
	v_exp_f32_e32 v23, v30
	v_add_f32_e32 v27, 1.0, v140
	v_fmac_f32_e32 v24, v20, v24
	v_fmac_f32_e32 v26, v22, v26
	v_fmac_f32_e32 v19, v18, v19
	v_fmac_f32_e32 v27, v23, v27
	v_rcp_f32_e32 v18, v24
	v_rcp_f32_e32 v22, v27
	v_rcp_f32_e32 v19, v19
	v_rcp_f32_e32 v23, v26
	v_exp_f32_e32 v146, v21
	v_exp_f32_e32 v147, v25
	s_mov_b32 s8, 0xc038aa3b
	s_mov_b32 s4, 0x4038aa3b
	v_mov_b64_e32 v[160:161], s[8:9]
	v_exp_f32_e32 v148, v29
	v_exp_f32_e32 v149, v33
	v_pk_fma_f32 v[20:21], v[138:139], s[4:5], v[160:161] op_sel_hi:[1,0,0]
	s_nop 0
	v_pk_mul_f32 v[214:215], v[20:21], v[18:19]
	v_pk_fma_f32 v[18:19], v[140:141], s[4:5], v[160:161] op_sel_hi:[1,0,0]
	s_nop 0
	v_pk_mul_f32 v[212:213], v[18:19], v[22:23]
	v_add_u32_e32 v231, s7, v229
	ds_read_b128 v[18:21], v231 offset:36928
	ds_read_b128 v[22:25], v231 offset:36944
	ds_read_b128 v[26:29], v231 offset:36960
	ds_read_b128 v[30:33], v231 offset:36976
	s_waitcnt lgkmcnt(5)
	v_mfma_f32_32x32x16_bf16 v[2:17], v[46:49], v[142:145], v[236:251]
	ds_read_b128 v[138:141], v159 offset:16384
	v_add_f32_e32 v162, 1.0, v146
	v_exp_f32_e32 v163, v215
	v_exp_f32_e32 v164, v214
	v_exp_f32_e32 v165, v213
	v_exp_f32_e32 v166, v212
	v_add_f32_e32 v142, 1.0, v147
	v_add_f32_e32 v143, 1.0, v148
	v_add_f32_e32 v144, 1.0, v149
	v_mfma_f32_32x32x16_bf16 v[2:17], v[42:45], v[130:133], v[2:17]
	ds_read_b128 v[146:149], v159 offset:16416
	v_fmac_f32_e32 v162, v162, v163
	v_fmac_f32_e32 v142, v142, v164
	v_fmac_f32_e32 v143, v143, v165
	v_fmac_f32_e32 v144, v144, v166
	v_mfma_f32_32x32x16_bf16 v[2:17], v[38:41], v[154:157], v[2:17]
	ds_read_b128 v[150:153], v159 offset:16448
	v_rcp_f32_e32 v130, v162
	v_rcp_f32_e32 v131, v142
	v_rcp_f32_e32 v132, v143
	v_rcp_f32_e32 v133, v144
	s_waitcnt vmcnt(16)
	v_mfma_f32_32x32x16_bf16 v[2:17], v[34:37], v[134:137], v[2:17]
	ds_read_b128 v[178:181], v159 offset:16480
	v_fma_f32 v130, -v163, v130, v130
	v_fma_f32 v131, -v164, v131, v131
	v_fma_f32 v132, -v165, v132, v132
	v_fma_f32 v133, -v166, v133, v133
	v_add_u32_e32 v211, s6, v210
	v_cvt_pk_bf16_f32 v252, v130, v131
	v_cvt_pk_bf16_f32 v253, v132, v133
	s_nop 3
	v_exp_f32_e32 v131, v4
	v_exp_f32_e32 v130, v8
	v_exp_f32_e32 v133, v12
	v_exp_f32_e32 v132, v16
	v_exp_f32_e32 v2, v2
	v_exp_f32_e32 v4, v6
	v_exp_f32_e32 v6, v10
	v_exp_f32_e32 v7, v14
	v_add_f32_e32 v3, 1.0, v131
	v_add_f32_e32 v8, 1.0, v130
	v_add_f32_e32 v10, 1.0, v133
	v_add_f32_e32 v11, 1.0, v132
	v_fmac_f32_e32 v3, v2, v3
	v_fmac_f32_e32 v8, v4, v8
	v_fmac_f32_e32 v10, v6, v10
	v_fmac_f32_e32 v11, v7, v11
	v_rcp_f32_e32 v3, v3
	v_rcp_f32_e32 v2, v8
	v_rcp_f32_e32 v7, v10
	v_rcp_f32_e32 v6, v11
	v_exp_f32_e32 v134, v5
	v_exp_f32_e32 v135, v9
	v_pk_fma_f32 v[4:5], v[130:131], s[4:5], v[160:161] op_sel_hi:[1,0,0]
	v_exp_f32_e32 v130, v13
	v_pk_mul_f32 v[204:205], v[4:5], v[2:3]
	v_pk_fma_f32 v[2:3], v[132:133], s[4:5], v[160:161] op_sel_hi:[1,0,0]
	v_exp_f32_e32 v131, v17
	v_pk_mul_f32 v[202:203], v[2:3], v[6:7]
	s_waitcnt lgkmcnt(3)
	v_mfma_f32_32x32x16_bf16 v[18:33], v[94:97], v[138:141], v[18:33]
	v_add_f32_e32 v132, 1.0, v134
	v_exp_f32_e32 v133, v205
	v_add_f32_e32 v134, 1.0, v135
	v_exp_f32_e32 v135, v204
	v_exp_f32_e32 v136, v203
	v_exp_f32_e32 v137, v202
	v_add_f32_e32 v130, 1.0, v130
	v_add_f32_e32 v131, 1.0, v131
	s_waitcnt lgkmcnt(2)
	v_mfma_f32_32x32x16_bf16 v[18:33], v[90:93], v[146:149], v[18:33]
	v_fmac_f32_e32 v132, v132, v133
	v_fmac_f32_e32 v134, v134, v135
	v_fmac_f32_e32 v130, v130, v136
	v_fmac_f32_e32 v131, v131, v137
	s_waitcnt lgkmcnt(1)
	v_mfma_f32_32x32x16_bf16 v[18:33], v[86:89], v[150:153], v[18:33]
	v_rcp_f32_e32 v132, v132
	v_rcp_f32_e32 v134, v134
	v_rcp_f32_e32 v130, v130
	v_rcp_f32_e32 v131, v131
	s_waitcnt lgkmcnt(0)
	v_mfma_f32_32x32x16_bf16 v[18:33], v[82:85], v[178:181], v[18:33]
	v_fma_f32 v132, -v133, v132, v132
	v_fma_f32 v133, -v135, v134, v134
	v_fma_f32 v134, -v136, v130, v130
	v_fma_f32 v131, -v137, v131, v131
	v_cvt_pk_bf16_f32 v254, v132, v133
	v_cvt_pk_bf16_f32 v255, v134, v131
	ds_write_b128 v211, v[252:255] offset:0
	s_waitcnt lgkmcnt(0)
	s_barrier
	s_setprio 1
	s_load_dwordx8 s[4:11], s[0:1], 0x10
	ds_read_b32 v229, v228 offset:31168
	ds_read_b128 v[174:177], v210
	v_add_u32_e32 v183, v230, v158
	ds_read_b128 v[170:173], v210 offset:1024
	v_exp_f32_e32 v131, v20
	v_exp_f32_e32 v130, v24
	v_exp_f32_e32 v133, v28
	v_exp_f32_e32 v132, v32
	ds_read_b128 v[166:169], v210 offset:2048
	v_exp_f32_e32 v18, v18
	v_exp_f32_e32 v20, v22
	v_exp_f32_e32 v22, v26
	v_exp_f32_e32 v23, v30
	v_fma_f32 v19, v131, s12, s12
	v_fma_f32 v24, v130, s12, s12
	v_fma_f32 v26, v133, s12, s12
	v_fma_f32 v27, v132, s12, s12
	ds_read_b128 v[162:165], v210 offset:3072
	v_fmac_f32_e32 v19, v18, v19
	v_fmac_f32_e32 v24, v20, v24
	v_fmac_f32_e32 v26, v22, v26
	v_fmac_f32_e32 v27, v23, v27
	ds_read_b128 v[158:161], v210 offset:4096
	v_rcp_f32_e32 v19, v19
	v_rcp_f32_e32 v18, v24
	v_rcp_f32_e32 v23, v26
	v_rcp_f32_e32 v22, v27
	ds_read_b128 v[154:157], v210 offset:5120
	v_exp_f32_e32 v186, v21
	v_exp_f32_e32 v187, v25
	ds_read_b128 v[142:145], v210 offset:6144
	s_mov_b32 s0, 0xc038aa3b
	v_exp_f32_e32 v188, v29
	v_pk_fma_f32 v[200:201], v[130:131], v[18:19], v[18:19] neg_lo:[1,0,0] neg_hi:[1,0,0]
	v_exp_f32_e32 v189, v33
	v_pk_fma_f32 v[198:199], v[132:133], v[22:23], v[22:23] neg_lo:[1,0,0] neg_hi:[1,0,0]
	ds_read_b128 v[130:133], v210 offset:7168
	ds_read_b128 v[18:21], v231 offset:36928
	ds_read_b128 v[22:25], v231 offset:36944
	ds_read_b128 v[26:29], v231 offset:36960
	ds_read_b128 v[30:33], v231 offset:36976
	v_mfma_f32_32x32x16_bf16 v[2:17], v[46:49], v[138:141], v[236:251]
	ds_read_b128 v[134:137], v183 offset:16384
	v_add_f32_e32 v186, 1.0, v186
	v_exp_f32_e32 v190, v201
	v_exp_f32_e32 v191, v200
	v_exp_f32_e32 v192, v199
	v_exp_f32_e32 v193, v198
	v_add_f32_e32 v187, 1.0, v187
	v_add_f32_e32 v188, 1.0, v188
	v_add_f32_e32 v189, 1.0, v189
	v_mfma_f32_32x32x16_bf16 v[2:17], v[42:45], v[146:149], v[2:17]
	ds_read_b128 v[138:141], v183 offset:16416
	v_fmac_f32_e32 v186, v186, v190
	v_fmac_f32_e32 v187, v187, v191
	v_fmac_f32_e32 v188, v188, v192
	v_fmac_f32_e32 v189, v189, v193
	v_mfma_f32_32x32x16_bf16 v[2:17], v[38:41], v[150:153], v[2:17]
	ds_read_b128 v[146:149], v183 offset:16448
	v_rcp_f32_e32 v186, v186
	v_rcp_f32_e32 v187, v187
	v_rcp_f32_e32 v188, v188
	v_rcp_f32_e32 v189, v189
	v_mfma_f32_32x32x16_bf16 v[2:17], v[34:37], v[178:181], v[2:17]
	ds_read_b128 v[150:153], v183 offset:16480
	v_fma_f32 v183, -v190, v186, v186
	v_fma_f32 v186, -v191, v187, v187
	v_fma_f32 v187, -v192, v188, v188
	v_fma_f32 v188, -v193, v189, v189
	s_waitcnt vmcnt(15) lgkmcnt(0)
	v_mfma_f32_32x32x16_bf16 v[18:33], v[126:129], v[174:177], v[18:33]
	v_cvt_pk_bf16_f32 v252, v183, v186
	v_cvt_pk_bf16_f32 v253, v187, v188
	s_waitcnt vmcnt(14)
	v_mfma_f32_32x32x16_bf16 v[18:33], v[122:125], v[170:173], v[18:33]
	s_nop 0
	v_exp_f32_e32 v179, v4
	v_exp_f32_e32 v178, v8
	v_exp_f32_e32 v181, v12
	v_exp_f32_e32 v180, v16
	s_waitcnt vmcnt(13)
	v_mfma_f32_32x32x16_bf16 v[18:33], v[118:121], v[166:169], v[18:33]
	v_exp_f32_e32 v2, v2
	v_exp_f32_e32 v4, v6
	v_exp_f32_e32 v7, v10
	v_exp_f32_e32 v8, v14
	v_fma_f32 v3, v179, s12, s12
	v_fma_f32 v6, v178, s12, s12
	v_fma_f32 v10, v181, s12, s12
	v_fma_f32 v11, v180, s12, s12
	s_waitcnt vmcnt(12)
	v_mfma_f32_32x32x16_bf16 v[18:33], v[114:117], v[162:165], v[18:33]
	v_fmac_f32_e32 v3, v2, v3
	v_fmac_f32_e32 v6, v4, v6
	v_fmac_f32_e32 v10, v7, v10
	v_fmac_f32_e32 v11, v8, v11
	s_waitcnt vmcnt(11)
	v_mfma_f32_32x32x16_bf16 v[18:33], v[110:113], v[158:161], v[18:33]
	v_rcp_f32_e32 v3, v3
	v_rcp_f32_e32 v2, v6
	v_rcp_f32_e32 v7, v10
	v_rcp_f32_e32 v6, v11
	s_waitcnt vmcnt(10)
	v_mfma_f32_32x32x16_bf16 v[18:33], v[106:109], v[154:157], v[18:33]
	v_exp_f32_e32 v183, v5
	v_exp_f32_e32 v186, v9
	s_waitcnt vmcnt(9)
	v_mfma_f32_32x32x16_bf16 v[18:33], v[102:105], v[142:145], v[18:33]
	v_pk_fma_f32 v[206:207], v[178:179], v[2:3], v[2:3] neg_lo:[1,0,0] neg_hi:[1,0,0]
	v_exp_f32_e32 v178, v13
	v_exp_f32_e32 v179, v17
	v_pk_fma_f32 v[208:209], v[180:181], v[6:7], v[6:7] neg_lo:[1,0,0] neg_hi:[1,0,0]
	s_waitcnt vmcnt(8)
	v_mfma_f32_32x32x16_bf16 v[18:33], v[98:101], v[130:133], v[18:33]
	v_mfma_f32_32x32x16_bf16 v[18:33], v[94:97], v[134:137], v[18:33]
	v_add_f32_e32 v180, 1.0, v183
	v_exp_f32_e32 v181, v207
	v_add_f32_e32 v183, 1.0, v186
	v_exp_f32_e32 v184, v206
	v_exp_f32_e32 v185, v209
	v_exp_f32_e32 v186, v208
	v_add_f32_e32 v178, 1.0, v178
	v_add_f32_e32 v179, 1.0, v179
	v_mfma_f32_32x32x16_bf16 v[18:33], v[90:93], v[138:141], v[18:33]
	v_fmac_f32_e32 v180, v180, v181
	v_fmac_f32_e32 v183, v183, v184
	v_fmac_f32_e32 v178, v178, v185
	v_fmac_f32_e32 v179, v179, v186
	v_mfma_f32_32x32x16_bf16 v[18:33], v[86:89], v[146:149], v[18:33]
	v_rcp_f32_e32 v180, v180
	v_rcp_f32_e32 v183, v183
	v_rcp_f32_e32 v178, v178
	v_rcp_f32_e32 v179, v179
	v_mfma_f32_32x32x16_bf16 v[18:33], v[82:85], v[150:153], v[18:33]
	v_fma_f32 v180, -v181, v180, v180
	v_fma_f32 v181, -v184, v183, v183
	v_fma_f32 v183, -v185, v178, v178
	v_fma_f32 v179, -v186, v179, v179
	v_cvt_pk_bf16_f32 v254, v180, v181
	v_cvt_pk_bf16_f32 v255, v183, v179
	ds_write_b128 v211, v[252:255] offset:8192
	s_waitcnt lgkmcnt(0)
	s_barrier
	v_mov_b32_e32 v178, 0x7a40
	v_lshl_add_u32 v232, v182, 2, v178
	s_mov_b32 s1, -1
	s_waitcnt vmcnt(0)
	s_branch .LBB1_14
